# v14 + router f32-MFMA matmul loops rewritten with dwordx4 B loads, 8 loads in flight across iterations (expert column mapping 4n+jt)
# speedup vs baseline: 1.0193x; 1.0193x over previous
; #define LAS __attribute__((address_space(3)))
; template <int NT>
; __device__ __forceinline__ void rows16_matmul(const LAS float* hfs, const float* W, int ldw, int col0, int wave, int lane, f32x4 (&acc)[NT]) {
; #pragma unroll
;     for (int jt = 0; jt < NT; ++jt) acc[jt] = (f32x4){0.f, 0.f, 0.f, 0.f};
;     const LAS float* ap = hfs + (lane & 15) * HFS_LD + wave * 256 + (lane >> 4);
;     const float* bp = W + (size_t)(wave * 256 + (lane >> 4)) * ldw + col0 + (lane & 15);
; #pragma unroll 8
;     for (int s4 = 0; s4 < 64; ++s4) {
;         const float a = ap[s4 * 4];
;         float b[NT];
; #pragma unroll
;         for (int jt = 0; jt < NT; ++jt) b[jt] = bp[(size_t)(s4 * 4) * ldw + jt * 16];
; #pragma unroll
;         for (int jt = 0; jt < NT; ++jt) acc[jt] = __builtin_amdgcn_mfma_f32_16x16x4f32(a, b[jt], acc[jt], 0, 0, 0);
;     }
; }
.Lrt0_pre:
	v_and_b32_e32 v250, 15, v1
	v_mul_u32_u24_e32 v250, 12, v250
	v_mov_b32_e32 v251, 0
	v_lshl_add_u64 v[248:249], v[18:19], 0, v[250:251]
	v_mov_b32_e32 v250, 0x1000
	v_lshl_add_u64 v[252:253], v[248:249], 0, v[250:251]
	s_mov_b32 s0, 0
	global_load_dwordx4 v[208:211], v[248:249], off
	global_load_dwordx4 v[212:215], v[248:249], off offset:1024
	global_load_dwordx4 v[216:219], v[248:249], off offset:2048
	global_load_dwordx4 v[220:223], v[248:249], off offset:3072
	global_load_dwordx4 v[224:227], v[252:253], off
	global_load_dwordx4 v[228:231], v[252:253], off offset:1024
	global_load_dwordx4 v[232:235], v[252:253], off offset:2048
	global_load_dwordx4 v[236:239], v[252:253], off offset:3072
.Lrt0_loop:
	ds_read2_b32 v[240:241], v20 offset1:4
	ds_read2_b32 v[242:243], v20 offset0:8 offset1:12
	ds_read2_b32 v[244:245], v20 offset0:16 offset1:20
	ds_read2_b32 v[246:247], v20 offset0:24 offset1:28
	v_add_u32_e32 v20, 0x80, v20
	s_add_u32 s0, s0, 0x2000
	s_cmp_lg_u32 s0, 0x10000
	s_cselect_b32 s2, 0x2000, 0
	v_mov_b32_e32 v250, s2
	v_lshl_add_u64 v[248:249], v[248:249], 0, v[250:251]
	v_lshl_add_u64 v[252:253], v[252:253], 0, v[250:251]
	s_waitcnt vmcnt(7) lgkmcnt(3)
	v_mfma_f32_16x16x4_f32 v[14:17], v240, v208, v[14:17]
	v_mfma_f32_16x16x4_f32 v[10:13], v240, v209, v[10:13]
	v_mfma_f32_16x16x4_f32 v[6:9], v240, v210, v[6:9]
	v_mfma_f32_16x16x4_f32 v[2:5], v240, v211, v[2:5]
	global_load_dwordx4 v[208:211], v[248:249], off
	s_waitcnt vmcnt(7) lgkmcnt(3)
	v_mfma_f32_16x16x4_f32 v[14:17], v241, v212, v[14:17]
	v_mfma_f32_16x16x4_f32 v[10:13], v241, v213, v[10:13]
	v_mfma_f32_16x16x4_f32 v[6:9], v241, v214, v[6:9]
	v_mfma_f32_16x16x4_f32 v[2:5], v241, v215, v[2:5]
	global_load_dwordx4 v[212:215], v[248:249], off offset:1024
	s_waitcnt vmcnt(7) lgkmcnt(2)
	v_mfma_f32_16x16x4_f32 v[14:17], v242, v216, v[14:17]
	v_mfma_f32_16x16x4_f32 v[10:13], v242, v217, v[10:13]
	v_mfma_f32_16x16x4_f32 v[6:9], v242, v218, v[6:9]
	v_mfma_f32_16x16x4_f32 v[2:5], v242, v219, v[2:5]
	global_load_dwordx4 v[216:219], v[248:249], off offset:2048
	s_waitcnt vmcnt(7) lgkmcnt(2)
	v_mfma_f32_16x16x4_f32 v[14:17], v243, v220, v[14:17]
	v_mfma_f32_16x16x4_f32 v[10:13], v243, v221, v[10:13]
	v_mfma_f32_16x16x4_f32 v[6:9], v243, v222, v[6:9]
	v_mfma_f32_16x16x4_f32 v[2:5], v243, v223, v[2:5]
	global_load_dwordx4 v[220:223], v[248:249], off offset:3072
	s_waitcnt vmcnt(7) lgkmcnt(1)
	v_mfma_f32_16x16x4_f32 v[14:17], v244, v224, v[14:17]
	v_mfma_f32_16x16x4_f32 v[10:13], v244, v225, v[10:13]
	v_mfma_f32_16x16x4_f32 v[6:9], v244, v226, v[6:9]
	v_mfma_f32_16x16x4_f32 v[2:5], v244, v227, v[2:5]
	global_load_dwordx4 v[224:227], v[252:253], off
	s_waitcnt vmcnt(7) lgkmcnt(1)
	v_mfma_f32_16x16x4_f32 v[14:17], v245, v228, v[14:17]
	v_mfma_f32_16x16x4_f32 v[10:13], v245, v229, v[10:13]
	v_mfma_f32_16x16x4_f32 v[6:9], v245, v230, v[6:9]
	v_mfma_f32_16x16x4_f32 v[2:5], v245, v231, v[2:5]
	global_load_dwordx4 v[228:231], v[252:253], off offset:1024
	s_waitcnt vmcnt(7) lgkmcnt(0)
	v_mfma_f32_16x16x4_f32 v[14:17], v246, v232, v[14:17]
	v_mfma_f32_16x16x4_f32 v[10:13], v246, v233, v[10:13]
	v_mfma_f32_16x16x4_f32 v[6:9], v246, v234, v[6:9]
	v_mfma_f32_16x16x4_f32 v[2:5], v246, v235, v[2:5]
	global_load_dwordx4 v[232:235], v[252:253], off offset:2048
	s_waitcnt vmcnt(7) lgkmcnt(0)
	v_mfma_f32_16x16x4_f32 v[14:17], v247, v236, v[14:17]
	v_mfma_f32_16x16x4_f32 v[10:13], v247, v237, v[10:13]
	v_mfma_f32_16x16x4_f32 v[6:9], v247, v238, v[6:9]
	v_mfma_f32_16x16x4_f32 v[2:5], v247, v239, v[2:5]
	global_load_dwordx4 v[236:239], v[252:253], off offset:3072
	s_cbranch_scc1 .Lrt0_loop
	s_waitcnt vmcnt(0)
	s_nop 7
	v_lshlrev_b32_e32 v18, 6, v1
	v_and_b32_e32 v18, 0xc00, v18
	v_lshl_or_b32 v18, v166, 12, v18
	v_add3_u32 v18, 0, v130, v18
	v_readlane_b32 s0, v254, 35
	s_barrier
; __device__ __forceinline__ void route_phase(LAS unsigned char* lds, int bid, int G, const float* x, const float* g, const float* sc, const float* sh,
;                                             const float* rw, const float* rbias, bf16_t* hbuf, int* cnt, int* list, u32x2* rec) {
;     ...
; #pragma unroll
;         for (int jt = 0; jt < 4; ++jt)
; #pragma unroll
;             for (int r = 0; r < 4; ++r) part[(wave * 16 + (lane >> 4) * 4 + r) * 64 + jt * 16 + (lane & 15)] = acc[jt][r];
;         __syncthreads();
; #pragma unroll 1
;         for (int rr = 0; rr < 2; ++rr) {
;             const int rl = wave * 2 + rr, row = r0 + rl;
;             float logit = 0.f;
; #pragma unroll
;             for (int w = 0; w < 8; ++w) logit += part[(w * 16 + rl) * 64 + lane];
;             const float score = 1.f / (1.f + expf(-logit));
;             const float sel = score + rbias[lane];
;             float m1 = sel; m1 = fmaxf(m1, __shfl_xor(m1, 1)); m1 = fmaxf(m1, __shfl_xor(m1, 2)); m1 = fmaxf(m1, __shfl_xor(m1, 4));
;             const unsigned long long bal = __ballot(sel == m1);
;             const unsigned gbits = (unsigned)(bal >> (lane & ~7)) & 0xffu;
;             const int idx1 = (lane & ~7) + __ffs(gbits) - 1;
;             float m2 = (lane == idx1) ? -INFINITY : sel; m2 = fmaxf(m2, __shfl_xor(m2, 1)); m2 = fmaxf(m2, __shfl_xor(m2, 2)); m2 = fmaxf(m2, __shfl_xor(m2, 4));
;             const float gs = m1 + m2;
;             const int grp = lane >> 3; int grank = 0;
; #pragma unroll
;             for (int gp = 0; gp < 8; ++gp) { const float o = __shfl(gs, gp * 8); grank += ((o > gs) || (o == gs && gp < grp)) ? 1 : 0; }
;             const bool elig = grank < 4;
;             const float sm = elig ? sel : -INFINITY;
;             int rank = 0;
; #pragma unroll
;             for (int j = 0; j < 64; ++j) { const float o = __builtin_bit_cast(float, __builtin_amdgcn_readlane(__builtin_bit_cast(int, sm), j)); rank += ((o > sm) || (o == sm && j < lane)) ? 1 : 0; }
	v_and_b32_e32 v250, 15, v1
	v_mad_u32_u24 v18, v250, 12, v18
	ds_write2_b32 v18, v14, v10 offset0:0 offset1:1
	ds_write2_b32 v18, v15, v11 offset0:64 offset1:65
	ds_write2_b32 v18, v16, v12 offset0:128 offset1:129
	ds_write2_b32 v18, v17, v13 offset0:192 offset1:193
	ds_write2_b32 v18, v6, v2 offset0:2 offset1:3
	ds_write2_b32 v18, v7, v3 offset0:66 offset1:67
	ds_write2_b32 v18, v8, v4 offset0:130 offset1:131
	ds_write2_b32 v18, v9, v5 offset0:194 offset1:195
	v_lshlrev_b32_e32 v130, 2, v159
	v_and_b32_e32 v4, 56, v1
	v_readlane_b32 s1, v254, 36
	v_lshlrev_b32_e32 v10, 2, v148
	v_lshlrev_b64 v[12:13], v159, -1
	v_lshl_add_u64 v[6:7], s[0:1], 0, v[130:131]
	v_cmp_eq_u32_e64 s[0:1], 56, v4
	v_add_u32_e32 v5, 0, v130
	v_lshl_add_u64 v[2:3], s[6:7], 0, v[130:131]
	v_writelane_b32 v254, s0, 48
	v_add_u32_e32 v9, -1, v4
	v_lshlrev_b32_e32 v11, 13, v159
	v_writelane_b32 v254, s1, 49
	v_cmp_ne_u32_e64 s[0:1], 0, v159
	v_not_b32_e32 v1, v13
	v_not_b32_e32 v8, v12
	v_writelane_b32 v254, s0, 50
	v_cmp_lt_u32_e64 s[8:9], 7, v159
	v_or_b32_e32 v12, 32, v10
	v_writelane_b32 v254, s1, 51
	v_cmp_lt_u32_e64 s[0:1], 1, v159
	v_cmp_lt_u32_e64 s[10:11], 15, v159
	v_or_b32_e32 v13, 64, v10
	v_writelane_b32 v254, s0, 52
	v_cmp_lt_u32_e64 s[12:13], 23, v159
	v_or_b32_e32 v14, 0x60, v10
	v_writelane_b32 v254, s1, 53
	v_cmp_lt_u32_e64 s[0:1], 2, v159
	v_cmp_lt_u32_e64 s[14:15], 31, v159
	v_or_b32_e32 v15, 0x80, v10
	v_writelane_b32 v254, s0, 54
	v_cmp_lt_u32_e64 s[16:17], 39, v159
	v_or_b32_e32 v16, 0xa0, v10
	v_writelane_b32 v254, s1, 55
	v_cmp_lt_u32_e64 s[0:1], 3, v159
	v_cmp_lt_u32_e64 s[18:19], 47, v159
	v_or_b32_e32 v17, 0xc0, v10
	v_writelane_b32 v254, s0, 56
	v_or_b32_e32 v18, 0xe0, v10
	s_mov_b32 s54, 0
	v_writelane_b32 v254, s1, 57
	v_cmp_lt_u32_e64 s[0:1], 4, v159
	v_cmp_lt_u32_e64 s[62:63], 21, v159
	v_cmp_lt_u32_e64 s[64:65], 22, v159
	v_writelane_b32 v254, s0, 58
	v_cmp_lt_u32_e64 s[66:67], 24, v159
	v_cmp_lt_u32_e64 s[68:69], 25, v159
	v_writelane_b32 v254, s1, 59
	v_cmp_lt_u32_e64 s[0:1], 5, v159
	v_cmp_lt_u32_e64 s[70:71], 26, v159
	v_cmp_lt_u32_e64 s[72:73], 27, v159
	v_writelane_b32 v254, s0, 60
	v_cmp_lt_u32_e64 s[74:75], 28, v159
	v_cmp_lt_u32_e64 s[76:77], 29, v159
	v_writelane_b32 v254, s1, 61
	v_cmp_lt_u32_e64 s[0:1], 6, v159
	v_cmp_lt_u32_e64 s[78:79], 30, v159
	v_cmp_lt_u32_e64 s[80:81], 32, v159
	v_writelane_b32 v254, s0, 62
	v_cmp_lt_u32_e64 s[82:83], 33, v159
	v_cmp_lt_u32_e64 s[84:85], 34, v159
	v_writelane_b32 v254, s1, 63
	v_cmp_lt_u32_e64 s[0:1], 8, v159
	v_cmp_lt_u32_e64 s[86:87], 35, v159
	v_cmp_lt_u32_e64 s[88:89], 36, v159
	v_writelane_b32 v255, s0, 0
	v_cmp_lt_u32_e64 s[90:91], 37, v159
	v_cmp_lt_u32_e64 s[92:93], 38, v159
	v_writelane_b32 v255, s1, 1
	v_cmp_lt_u32_e64 s[0:1], 9, v159
	v_cmp_lt_u32_e64 s[94:95], 40, v159
	v_cmp_lt_u32_e64 s[96:97], 41, v159
	v_writelane_b32 v255, s0, 2
	v_cmp_lt_u32_e64 s[6:7], 42, v159
	v_cmp_lt_u32_e64 s[4:5], 43, v159
	v_writelane_b32 v255, s1, 3
	v_cmp_lt_u32_e64 s[0:1], 10, v159
	v_cmp_lt_u32_e64 s[20:21], 44, v159
	v_cmp_lt_u32_e64 s[2:3], 45, v159
	v_writelane_b32 v255, s0, 4
	v_cmp_lt_u32_e64 s[22:23], 48, v159
	v_cmp_lt_u32_e64 s[24:25], 49, v159
	v_writelane_b32 v255, s1, 5
	v_cmp_lt_u32_e64 s[0:1], 11, v159
	v_cmp_lt_u32_e64 s[26:27], 50, v159
	v_cmp_lt_u32_e64 s[28:29], 51, v159
	v_writelane_b32 v255, s0, 6
	v_cmp_lt_u32_e64 s[30:31], 52, v159
	v_cmp_lt_u32_e64 s[34:35], 53, v159
	v_writelane_b32 v255, s1, 7
	v_cmp_lt_u32_e64 s[0:1], 12, v159
	v_cmp_lt_u32_e64 s[36:37], 54, v159
	v_cmp_lt_u32_e64 s[38:39], 55, v159
	v_writelane_b32 v255, s0, 8
	v_cmp_lt_u32_e64 s[40:41], 56, v159
	v_cmp_lt_u32_e64 s[42:43], 57, v159
	v_writelane_b32 v255, s1, 9
	v_cmp_lt_u32_e64 s[0:1], 13, v159
	v_cmp_lt_u32_e64 s[44:45], 58, v159
	v_cmp_lt_u32_e64 s[46:47], 59, v159
	v_writelane_b32 v255, s0, 10
	v_cmp_lt_u32_e64 s[48:49], 60, v159
	v_cmp_lt_u32_e64 s[50:51], 61, v159
	v_writelane_b32 v255, s1, 11
	v_cmp_lt_u32_e64 s[0:1], 14, v159
	v_cmp_eq_u32_e64 s[52:53], 63, v159
	s_mov_b64 s[58:59], -1
	v_writelane_b32 v255, s0, 12
	s_waitcnt lgkmcnt(0)
	s_barrier
	v_writelane_b32 v255, s1, 13
	v_cmp_lt_u32_e64 s[0:1], 16, v159
	s_nop 1
	v_writelane_b32 v255, s0, 14
	s_nop 1
	v_writelane_b32 v255, s1, 15
	v_cmp_lt_u32_e64 s[0:1], 17, v159
	s_nop 1
	v_writelane_b32 v255, s0, 16
	s_nop 1
	v_writelane_b32 v255, s1, 17
	v_cmp_lt_u32_e64 s[0:1], 18, v159
	s_nop 1
	v_writelane_b32 v255, s0, 18
	s_nop 1
	v_writelane_b32 v255, s1, 19
	v_cmp_lt_u32_e64 s[0:1], 19, v159
	s_nop 1
	v_writelane_b32 v255, s0, 20
	s_nop 1
	v_writelane_b32 v255, s1, 21
	v_cmp_lt_u32_e64 s[0:1], 20, v159
	s_nop 1
	v_writelane_b32 v255, s0, 22
	s_nop 1
	v_writelane_b32 v255, s1, 23
	v_cmp_lt_u32_e64 s[0:1], 46, v159
	s_branch .LBB0_1007

; #define LAS __attribute__((address_space(3)))
; template <int NT>
; __device__ __forceinline__ void rows16_matmul(const LAS float* hfs, const float* W, int ldw, int col0, int wave, int lane, f32x4 (&acc)[NT]) {
; #pragma unroll
;     for (int jt = 0; jt < NT; ++jt) acc[jt] = (f32x4){0.f, 0.f, 0.f, 0.f};
;     const LAS float* ap = hfs + (lane & 15) * HFS_LD + wave * 256 + (lane >> 4);
;     const float* bp = W + (size_t)(wave * 256 + (lane >> 4)) * ldw + col0 + (lane & 15);
; #pragma unroll 8
;     for (int s4 = 0; s4 < 64; ++s4) {
;         const float a = ap[s4 * 4];
;         float b[NT];
; #pragma unroll
;         for (int jt = 0; jt < NT; ++jt) b[jt] = bp[(size_t)(s4 * 4) * ldw + jt * 16];
; #pragma unroll
;         for (int jt = 0; jt < NT; ++jt) acc[jt] = __builtin_amdgcn_mfma_f32_16x16x4f32(a, b[jt], acc[jt], 0, 0, 0);
;     }
; }
.Lrt1_pre:
	v_and_b32_e32 v250, 15, v1
	v_mul_u32_u24_e32 v250, 12, v250
	v_mov_b32_e32 v251, 0
	v_lshl_add_u64 v[248:249], v[18:19], 0, v[250:251]
	v_mov_b32_e32 v250, 0x80000
	v_lshl_add_u64 v[248:249], v[248:249], 0, v[250:251]
	v_mov_b32_e32 v250, 0x1000
	v_lshl_add_u64 v[252:253], v[248:249], 0, v[250:251]
	s_mov_b32 s0, 0
	global_load_dwordx4 v[208:211], v[248:249], off
	global_load_dwordx4 v[212:215], v[248:249], off offset:1024
	global_load_dwordx4 v[216:219], v[248:249], off offset:2048
	global_load_dwordx4 v[220:223], v[248:249], off offset:3072
	global_load_dwordx4 v[224:227], v[252:253], off
	global_load_dwordx4 v[228:231], v[252:253], off offset:1024
	global_load_dwordx4 v[232:235], v[252:253], off offset:2048
	global_load_dwordx4 v[236:239], v[252:253], off offset:3072
.Lrt1_loop:
	ds_read2_b32 v[240:241], v21 offset1:4
	ds_read2_b32 v[242:243], v21 offset0:8 offset1:12
	ds_read2_b32 v[244:245], v21 offset0:16 offset1:20
	ds_read2_b32 v[246:247], v21 offset0:24 offset1:28
	v_add_u32_e32 v21, 0x80, v21
	s_add_u32 s0, s0, 0x2000
	s_cmp_lg_u32 s0, 0x10000
	s_cselect_b32 s2, 0x2000, 0
	v_mov_b32_e32 v250, s2
	v_lshl_add_u64 v[248:249], v[248:249], 0, v[250:251]
	v_lshl_add_u64 v[252:253], v[252:253], 0, v[250:251]
	s_waitcnt vmcnt(7) lgkmcnt(3)
	v_mfma_f32_16x16x4_f32 v[14:17], v240, v208, v[14:17]
	v_mfma_f32_16x16x4_f32 v[10:13], v240, v209, v[10:13]
	v_mfma_f32_16x16x4_f32 v[6:9], v240, v210, v[6:9]
	v_mfma_f32_16x16x4_f32 v[2:5], v240, v211, v[2:5]
	global_load_dwordx4 v[208:211], v[248:249], off
	s_waitcnt vmcnt(7) lgkmcnt(3)
	v_mfma_f32_16x16x4_f32 v[14:17], v241, v212, v[14:17]
	v_mfma_f32_16x16x4_f32 v[10:13], v241, v213, v[10:13]
	v_mfma_f32_16x16x4_f32 v[6:9], v241, v214, v[6:9]
	v_mfma_f32_16x16x4_f32 v[2:5], v241, v215, v[2:5]
	global_load_dwordx4 v[212:215], v[248:249], off offset:1024
	s_waitcnt vmcnt(7) lgkmcnt(2)
	v_mfma_f32_16x16x4_f32 v[14:17], v242, v216, v[14:17]
	v_mfma_f32_16x16x4_f32 v[10:13], v242, v217, v[10:13]
	v_mfma_f32_16x16x4_f32 v[6:9], v242, v218, v[6:9]
	v_mfma_f32_16x16x4_f32 v[2:5], v242, v219, v[2:5]
	global_load_dwordx4 v[216:219], v[248:249], off offset:2048
	s_waitcnt vmcnt(7) lgkmcnt(2)
	v_mfma_f32_16x16x4_f32 v[14:17], v243, v220, v[14:17]
	v_mfma_f32_16x16x4_f32 v[10:13], v243, v221, v[10:13]
	v_mfma_f32_16x16x4_f32 v[6:9], v243, v222, v[6:9]
	v_mfma_f32_16x16x4_f32 v[2:5], v243, v223, v[2:5]
	global_load_dwordx4 v[220:223], v[248:249], off offset:3072
	s_waitcnt vmcnt(7) lgkmcnt(1)
	v_mfma_f32_16x16x4_f32 v[14:17], v244, v224, v[14:17]
	v_mfma_f32_16x16x4_f32 v[10:13], v244, v225, v[10:13]
	v_mfma_f32_16x16x4_f32 v[6:9], v244, v226, v[6:9]
	v_mfma_f32_16x16x4_f32 v[2:5], v244, v227, v[2:5]
	global_load_dwordx4 v[224:227], v[252:253], off
	s_waitcnt vmcnt(7) lgkmcnt(1)
	v_mfma_f32_16x16x4_f32 v[14:17], v245, v228, v[14:17]
	v_mfma_f32_16x16x4_f32 v[10:13], v245, v229, v[10:13]
	v_mfma_f32_16x16x4_f32 v[6:9], v245, v230, v[6:9]
	v_mfma_f32_16x16x4_f32 v[2:5], v245, v231, v[2:5]
	global_load_dwordx4 v[228:231], v[252:253], off offset:1024
	s_waitcnt vmcnt(7) lgkmcnt(0)
	v_mfma_f32_16x16x4_f32 v[14:17], v246, v232, v[14:17]
	v_mfma_f32_16x16x4_f32 v[10:13], v246, v233, v[10:13]
	v_mfma_f32_16x16x4_f32 v[6:9], v246, v234, v[6:9]
	v_mfma_f32_16x16x4_f32 v[2:5], v246, v235, v[2:5]
	global_load_dwordx4 v[232:235], v[252:253], off offset:2048
	s_waitcnt vmcnt(7) lgkmcnt(0)
	v_mfma_f32_16x16x4_f32 v[14:17], v247, v236, v[14:17]
	v_mfma_f32_16x16x4_f32 v[10:13], v247, v237, v[10:13]
	v_mfma_f32_16x16x4_f32 v[6:9], v247, v238, v[6:9]
	v_mfma_f32_16x16x4_f32 v[2:5], v247, v239, v[2:5]
	global_load_dwordx4 v[236:239], v[252:253], off offset:3072
	s_cbranch_scc1 .Lrt1_loop
	s_waitcnt vmcnt(0)
	s_nop 7
	v_lshlrev_b32_e32 v19, 6, v1
	v_and_b32_e32 v19, 0xc00, v19
	v_lshlrev_b32_e32 v18, 2, v20
	v_lshl_or_b32 v19, v172, 12, v19
	v_add3_u32 v18, 0, v18, v19
	v_readlane_b32 s0, v254, 35
	s_barrier
; __device__ __forceinline__ void route_phase(LAS unsigned char* lds, int bid, int G, const float* x, const float* g, const float* sc, const float* sh,
;                                             const float* rw, const float* rbias, bf16_t* hbuf, int* cnt, int* list, u32x2* rec) {
;     ...
; #pragma unroll
;         for (int jt = 0; jt < 4; ++jt)
; #pragma unroll
;             for (int r = 0; r < 4; ++r) part[(wave * 16 + (lane >> 4) * 4 + r) * 64 + jt * 16 + (lane & 15)] = acc[jt][r];
;         __syncthreads();
; #pragma unroll 1
;         for (int rr = 0; rr < 2; ++rr) {
;             const int rl = wave * 2 + rr, row = r0 + rl;
;             float logit = 0.f;
; #pragma unroll
;             for (int w = 0; w < 8; ++w) logit += part[(w * 16 + rl) * 64 + lane];
;             const float score = 1.f / (1.f + expf(-logit));
;             const float sel = score + rbias[lane];
;             float m1 = sel; m1 = fmaxf(m1, __shfl_xor(m1, 1)); m1 = fmaxf(m1, __shfl_xor(m1, 2)); m1 = fmaxf(m1, __shfl_xor(m1, 4));
;             const unsigned long long bal = __ballot(sel == m1);
;             const unsigned gbits = (unsigned)(bal >> (lane & ~7)) & 0xffu;
;             const int idx1 = (lane & ~7) + __ffs(gbits) - 1;
;             float m2 = (lane == idx1) ? -INFINITY : sel; m2 = fmaxf(m2, __shfl_xor(m2, 1)); m2 = fmaxf(m2, __shfl_xor(m2, 2)); m2 = fmaxf(m2, __shfl_xor(m2, 4));
;             const float gs = m1 + m2;
;             const int grp = lane >> 3; int grank = 0;
; #pragma unroll
;             for (int gp = 0; gp < 8; ++gp) { const float o = __shfl(gs, gp * 8); grank += ((o > gs) || (o == gs && gp < grp)) ? 1 : 0; }
;             const bool elig = grank < 4;
;             const float sm = elig ? sel : -INFINITY;
;             int rank = 0;
; #pragma unroll
;             for (int j = 0; j < 64; ++j) { const float o = __builtin_bit_cast(float, __builtin_amdgcn_readlane(__builtin_bit_cast(int, sm), j)); rank += ((o > sm) || (o == sm && j < lane)) ? 1 : 0; }
	v_and_b32_e32 v250, 15, v1
	v_mad_u32_u24 v18, v250, 12, v18
	ds_write2_b32 v18, v14, v10 offset0:0 offset1:1
	ds_write2_b32 v18, v15, v11 offset0:64 offset1:65
	ds_write2_b32 v18, v16, v12 offset0:128 offset1:129
	ds_write2_b32 v18, v17, v13 offset0:192 offset1:193
	ds_write2_b32 v18, v6, v2 offset0:2 offset1:3
	ds_write2_b32 v18, v7, v3 offset0:66 offset1:67
	ds_write2_b32 v18, v8, v4 offset0:130 offset1:131
	ds_write2_b32 v18, v9, v5 offset0:194 offset1:195
	v_lshlrev_b32_e32 v142, 2, v167
	v_and_b32_e32 v4, 56, v1
	v_readlane_b32 s1, v254, 36
	v_lshlrev_b32_e32 v10, 2, v156
	v_lshlrev_b64 v[12:13], v167, -1
	v_lshl_add_u64 v[6:7], s[0:1], 0, v[142:143]
	v_cmp_eq_u32_e64 s[0:1], 56, v4
	v_add_u32_e32 v5, 0, v142
	v_lshl_add_u64 v[2:3], s[10:11], 0, v[142:143]
	v_writelane_b32 v254, s0, 19
	v_add_u32_e32 v9, -1, v4
	v_lshlrev_b32_e32 v11, 13, v167
	v_writelane_b32 v254, s1, 20
	v_cmp_ne_u32_e64 s[0:1], 0, v167
	v_not_b32_e32 v1, v13
	v_not_b32_e32 v8, v12
	v_writelane_b32 v254, s0, 48
	v_cmp_lt_u32_e64 s[2:3], 7, v167
	v_or_b32_e32 v12, 32, v10
	v_writelane_b32 v254, s1, 49
	v_cmp_lt_u32_e64 s[0:1], 1, v167
	v_cmp_lt_u32_e64 s[6:7], 15, v167
	v_or_b32_e32 v13, 64, v10
	v_writelane_b32 v254, s0, 50
	v_cmp_lt_u32_e64 s[8:9], 23, v167
	v_or_b32_e32 v14, 0x60, v10
	v_writelane_b32 v254, s1, 51
	v_cmp_lt_u32_e64 s[0:1], 2, v167
	v_cmp_lt_u32_e64 s[10:11], 31, v167
	v_or_b32_e32 v15, 0x80, v10
	v_writelane_b32 v254, s0, 52
	v_cmp_lt_u32_e64 s[12:13], 39, v167
	v_or_b32_e32 v16, 0xa0, v10
	v_writelane_b32 v254, s1, 53
	v_cmp_lt_u32_e64 s[0:1], 3, v167
	v_cmp_lt_u32_e64 s[14:15], 47, v167
	v_or_b32_e32 v17, 0xc0, v10
	v_writelane_b32 v254, s0, 54
	v_or_b32_e32 v18, 0xe0, v10
	s_mov_b32 s50, 0
	v_writelane_b32 v254, s1, 55
	v_cmp_lt_u32_e64 s[0:1], 4, v167
	v_cmp_lt_u32_e64 s[58:59], 21, v167
	v_cmp_lt_u32_e64 s[60:61], 22, v167
	v_writelane_b32 v254, s0, 56
	v_cmp_lt_u32_e64 s[62:63], 24, v167
	v_cmp_lt_u32_e64 s[64:65], 25, v167
	v_writelane_b32 v254, s1, 57
	v_cmp_lt_u32_e64 s[0:1], 5, v167
	v_cmp_lt_u32_e64 s[66:67], 26, v167
	v_cmp_lt_u32_e64 s[68:69], 27, v167
	v_writelane_b32 v254, s0, 58
	v_cmp_lt_u32_e64 s[70:71], 28, v167
	v_cmp_lt_u32_e64 s[72:73], 29, v167
	v_writelane_b32 v254, s1, 59
	v_cmp_lt_u32_e64 s[0:1], 6, v167
	v_cmp_lt_u32_e64 s[74:75], 30, v167
	v_cmp_lt_u32_e64 s[76:77], 32, v167
	v_writelane_b32 v254, s0, 60
	v_cmp_lt_u32_e64 s[78:79], 33, v167
	v_cmp_lt_u32_e64 s[80:81], 34, v167
	v_writelane_b32 v254, s1, 61
	v_cmp_lt_u32_e64 s[0:1], 8, v167
	v_cmp_lt_u32_e64 s[82:83], 35, v167
	v_cmp_lt_u32_e64 s[84:85], 36, v167
	v_writelane_b32 v254, s0, 62
	v_cmp_lt_u32_e64 s[86:87], 37, v167
	v_cmp_lt_u32_e64 s[88:89], 38, v167
	v_writelane_b32 v254, s1, 63
	v_cmp_lt_u32_e64 s[0:1], 9, v167
	v_cmp_lt_u32_e64 s[90:91], 40, v167
	v_cmp_lt_u32_e64 s[92:93], 41, v167
	v_writelane_b32 v255, s0, 0
	v_cmp_lt_u32_e64 s[94:95], 42, v167
	v_cmp_lt_u32_e64 s[4:5], 43, v167
	v_writelane_b32 v255, s1, 1
	v_cmp_lt_u32_e64 s[0:1], 10, v167
	v_cmp_lt_u32_e64 s[96:97], 44, v167
	v_cmp_lt_u32_e64 s[16:17], 46, v167
	v_writelane_b32 v255, s0, 2
	v_cmp_lt_u32_e64 s[18:19], 48, v167
	v_cmp_lt_u32_e64 s[20:21], 49, v167
	v_writelane_b32 v255, s1, 3
	v_cmp_lt_u32_e64 s[0:1], 11, v167
	v_cmp_lt_u32_e64 s[22:23], 50, v167
	v_cmp_lt_u32_e64 s[24:25], 51, v167
	v_writelane_b32 v255, s0, 4
	v_cmp_lt_u32_e64 s[26:27], 52, v167
	v_cmp_lt_u32_e64 s[28:29], 53, v167
	v_writelane_b32 v255, s1, 5
	v_cmp_lt_u32_e64 s[0:1], 12, v167
	v_cmp_lt_u32_e64 s[30:31], 54, v167
	v_cmp_lt_u32_e64 s[34:35], 55, v167
	v_writelane_b32 v255, s0, 6
	v_cmp_lt_u32_e64 s[36:37], 56, v167
	v_cmp_lt_u32_e64 s[38:39], 57, v167
	v_writelane_b32 v255, s1, 7
	v_cmp_lt_u32_e64 s[0:1], 13, v167
	v_cmp_lt_u32_e64 s[40:41], 58, v167
	v_cmp_lt_u32_e64 s[42:43], 59, v167
	v_writelane_b32 v255, s0, 8
	v_cmp_lt_u32_e64 s[44:45], 60, v167
	v_cmp_lt_u32_e64 s[46:47], 61, v167
	v_writelane_b32 v255, s1, 9
	v_cmp_lt_u32_e64 s[0:1], 14, v167
	v_cmp_eq_u32_e64 s[48:49], 63, v167
	s_mov_b64 s[54:55], -1
	v_writelane_b32 v255, s0, 10
	s_waitcnt lgkmcnt(0)
	s_barrier
	v_writelane_b32 v255, s1, 11
	v_cmp_lt_u32_e64 s[0:1], 16, v167
	s_nop 1
	v_writelane_b32 v255, s0, 12
	s_nop 1
	v_writelane_b32 v255, s1, 13
	v_cmp_lt_u32_e64 s[0:1], 17, v167
	s_nop 1
	v_writelane_b32 v255, s0, 14
	s_nop 1
	v_writelane_b32 v255, s1, 15
	v_cmp_lt_u32_e64 s[0:1], 18, v167
	s_nop 1
	v_writelane_b32 v255, s0, 16
	s_nop 1
	v_writelane_b32 v255, s1, 17
	v_cmp_lt_u32_e64 s[0:1], 19, v167
	s_nop 1
	v_writelane_b32 v255, s0, 18
	s_nop 1
	v_writelane_b32 v255, s1, 19
	v_cmp_lt_u32_e64 s[0:1], 20, v167
	s_nop 1
	v_writelane_b32 v255, s0, 20
	s_nop 1
	v_writelane_b32 v255, s1, 21
	v_cmp_lt_u32_e64 s[0:1], 45, v167
	s_branch .LBB0_1744
